# conv mixer: 24 row loads per work item in flight (hoisted), on top of setprio removal
# baseline (speedup 1.0000x reference)
; __device__ __forceinline__ u32x4 pack8(const float (&v)[8]) { u32x4 w; w.x = pk2(v[0], v[1]); w.y = pk2(v[2], v[3]); w.z = pk2(v[4], v[5]); w.w = pk2(v[6], v[7]); return w; }
; __device__ __forceinline__ void ph_conv_hglocal(const Ctx& c) {
;     ...
;         for (int it = gtid; it < (T_ / 8) * 128; it += gn) {
;             const int c8 = it & 127, tb = it >> 7, t0 = tb * 8, ch = c8 * 8;
;             float w0[8], w1[8], w2[8];
; #pragma unroll
;             for (int j = 0; j < 8; ++j) { w0[j] = cw[ch + j]; w1[j] = cw[1024 + ch + j]; w2[j] = cw[2048 + ch + j]; }
;             float um2[8], um1[8];
; #pragma unroll
;             for (int j = 0; j < 8; ++j) { um2[j] = 0.f; um1[j] = 0.f; }
;             if ((t0 & (SEQ - 1)) != 0) {
;                 float a[8], b[8];
;                 unpack8(*(const u32x4*)(Z + (size_t)(t0 - 2) * NIN + 1024 + ch), a); unpack8(*(const u32x4*)(Z + (size_t)(t0 - 2) * NIN + 2048 + ch), b);
; #pragma unroll
;                 for (int j = 0; j < 8; ++j) um2[j] = a[j] * b[j];
;                 unpack8(*(const u32x4*)(Z + (size_t)(t0 - 1) * NIN + 1024 + ch), a); unpack8(*(const u32x4*)(Z + (size_t)(t0 - 1) * NIN + 2048 + ch), b);
; #pragma unroll
;                 for (int j = 0; j < 8; ++j) um1[j] = a[j] * b[j];
;             }
; #pragma unroll
;             for (int tt = 0; tt < 8; ++tt) {
;                 const size_t ro = (size_t)(t0 + tt) * NIN; float ab[8], ac[8], ah[8], o[8];
;                 unpack8(*(const u32x4*)(Z + ro + ch), ab); unpack8(*(const u32x4*)(Z + ro + 1024 + ch), ac); unpack8(*(const u32x4*)(Z + ro + 2048 + ch), ah);
; #pragma unroll
;                 for (int j = 0; j < 8; ++j) { const float u0 = ac[j] * ah[j]; o[j] = ab[j] * (w0[j] * um2[j] + w1[j] * um1[j] + w2[j] * u0); um2[j] = um1[j]; um1[j] = u0; }
;                 *(u32x4*)(Y + (size_t)(t0 + tt) * D_ + ch) = pack8(o);
;             }
.LBB0_450:
	s_or_b64 exec, exec, s[16:17]
	v_mov_b64_e32 v[32:33], s[4:5]
	v_mad_i64_i32 v[28:29], s[16:17], v30, s20, v[32:33]
	v_lshl_add_u64 v[28:29], v[28:29], 0, v[26:27]
	v_add_co_u32_e32 v196, vcc, 0x800, v28
	s_nop 1
	v_addc_co_u32_e32 v197, vcc, 0, v29, vcc
	global_load_dwordx4 v[100:103], v[196:197], off offset:-2048
	global_load_dwordx4 v[104:107], v[196:197], off
	global_load_dwordx4 v[108:111], v[196:197], off offset:2048
	v_add_co_u32_e32 v196, vcc, 0x4000, v28
	s_nop 1
	v_addc_co_u32_e32 v197, vcc, 0, v29, vcc
	global_load_dwordx4 v[112:115], v[196:197], off offset:-2048
	global_load_dwordx4 v[116:119], v[196:197], off
	global_load_dwordx4 v[120:123], v[196:197], off offset:2048
	v_add_co_u32_e32 v196, vcc, 0x7800, v28
	s_nop 1
	v_addc_co_u32_e32 v197, vcc, 0, v29, vcc
	global_load_dwordx4 v[124:127], v[196:197], off offset:-2048
	global_load_dwordx4 v[128:131], v[196:197], off
	global_load_dwordx4 v[132:135], v[196:197], off offset:2048
	v_add_co_u32_e32 v196, vcc, 0xb000, v28
	s_nop 1
	v_addc_co_u32_e32 v197, vcc, 0, v29, vcc
	global_load_dwordx4 v[136:139], v[196:197], off offset:-2048
	global_load_dwordx4 v[140:143], v[196:197], off
	global_load_dwordx4 v[144:147], v[196:197], off offset:2048
	v_add_co_u32_e32 v196, vcc, 0xe800, v28
	s_nop 1
	v_addc_co_u32_e32 v197, vcc, 0, v29, vcc
	global_load_dwordx4 v[148:151], v[196:197], off offset:-2048
	global_load_dwordx4 v[152:155], v[196:197], off
	global_load_dwordx4 v[156:159], v[196:197], off offset:2048
	v_add_co_u32_e32 v196, vcc, 0x12000, v28
	s_nop 1
	v_addc_co_u32_e32 v197, vcc, 0, v29, vcc
	global_load_dwordx4 v[160:163], v[196:197], off offset:-2048
	global_load_dwordx4 v[164:167], v[196:197], off
	global_load_dwordx4 v[168:171], v[196:197], off offset:2048
	v_add_co_u32_e32 v196, vcc, 0x15800, v28
	s_nop 1
	v_addc_co_u32_e32 v197, vcc, 0, v29, vcc
	global_load_dwordx4 v[172:175], v[196:197], off offset:-2048
	global_load_dwordx4 v[176:179], v[196:197], off
	global_load_dwordx4 v[180:183], v[196:197], off offset:2048
	v_add_co_u32_e32 v196, vcc, 0x19000, v28
	s_nop 1
	v_addc_co_u32_e32 v197, vcc, 0, v29, vcc
	global_load_dwordx4 v[184:187], v[196:197], off offset:-2048
	global_load_dwordx4 v[188:191], v[196:197], off
	global_load_dwordx4 v[192:195], v[196:197], off offset:2048
	s_nop 0
	v_add_co_u32_e32 v28, vcc, s19, v28
	v_ashrrev_i32_e32 v31, 31, v30
	s_nop 0
	v_addc_co_u32_e32 v29, vcc, 0, v29, vcc
	s_nop 0
	s_waitcnt vmcnt(21)
	v_mov_b32_e32 v54, v100
	v_mov_b32_e32 v55, v101
	v_mov_b32_e32 v56, v102
	v_mov_b32_e32 v57, v103
	v_mov_b32_e32 v58, v104
	v_mov_b32_e32 v59, v105
	v_mov_b32_e32 v60, v106
	v_mov_b32_e32 v61, v107
	v_mov_b32_e32 v62, v108
	v_mov_b32_e32 v63, v109
	v_mov_b32_e32 v64, v110
	v_mov_b32_e32 v65, v111
	v_pk_mul_f32 v[70:71], v[20:21], v[36:37]
	v_pk_mul_f32 v[72:73], v[22:23], v[34:35]
	v_or_b32_e32 v74, 1, v30
	v_lshl_add_u64 v[28:29], s[6:7], 0, v[26:27]
	v_pk_mul_f32 v[66:67], v[16:17], v[40:41]
	v_pk_mul_f32 v[68:69], v[18:19], v[38:39]
	v_pk_fma_f32 v[70:71], v[8:9], v[44:45], v[70:71]
	v_pk_fma_f32 v[72:73], v[10:11], v[42:43], v[72:73]
	v_lshlrev_b64 v[42:43], 12, v[30:31]
	v_mad_i64_i32 v[44:45], s[16:17], v74, s20, v[32:33]
	v_pk_fma_f32 v[66:67], v[12:13], v[48:49], v[66:67]
	v_pk_fma_f32 v[68:69], v[14:15], v[46:47], v[68:69]
	v_lshl_add_u64 v[76:77], v[28:29], 0, v[42:43]
	v_lshl_add_u64 v[78:79], v[44:45], 0, v[26:27]
	v_ashrrev_i32_e32 v75, 31, v74
	v_add_u32_e32 v25, s3, v25
	v_add_u32_e32 v51, s18, v51
	v_lshlrev_b32_e32 v80, 16, v54
	v_lshlrev_b32_e32 v42, 16, v58
	v_and_b32_e32 v43, 0xffff0000, v58
	v_lshlrev_b32_e32 v44, 16, v59
	v_and_b32_e32 v45, 0xffff0000, v59
	v_lshlrev_b32_e32 v46, 16, v60
	v_and_b32_e32 v47, 0xffff0000, v60
	v_lshlrev_b32_e32 v48, 16, v61
	v_and_b32_e32 v49, 0xffff0000, v61
	v_lshlrev_b32_e32 v60, 16, v62
	v_and_b32_e32 v61, 0xffff0000, v62
	v_lshlrev_b32_e32 v62, 16, v63
	v_and_b32_e32 v63, 0xffff0000, v63
	v_lshlrev_b32_e32 v82, 16, v64
	v_and_b32_e32 v83, 0xffff0000, v64
	v_lshlrev_b32_e32 v64, 16, v65
	v_and_b32_e32 v65, 0xffff0000, v65
	v_pk_mul_f32 v[42:43], v[42:43], v[60:61]
	v_pk_mul_f32 v[44:45], v[44:45], v[62:63]
	v_pk_mul_f32 v[46:47], v[46:47], v[82:83]
	v_pk_mul_f32 v[48:49], v[48:49], v[64:65]
	v_and_b32_e32 v81, 0xffff0000, v54
	v_lshlrev_b32_e32 v54, 16, v55
	v_and_b32_e32 v55, 0xffff0000, v55
	v_lshlrev_b32_e32 v58, 16, v56
	v_and_b32_e32 v59, 0xffff0000, v56
	v_lshlrev_b32_e32 v56, 16, v57
	v_and_b32_e32 v57, 0xffff0000, v57
	v_pk_fma_f32 v[60:61], v[4:5], v[42:43], v[66:67]
	v_pk_fma_f32 v[62:63], v[6:7], v[44:45], v[68:69]
	v_pk_fma_f32 v[64:65], v[0:1], v[46:47], v[70:71]
	v_pk_fma_f32 v[66:67], v[2:3], v[48:49], v[72:73]
	v_pk_mul_f32 v[60:61], v[60:61], v[80:81]
	v_pk_mul_f32 v[62:63], v[62:63], v[54:55]
	v_pk_mul_f32 v[58:59], v[64:65], v[58:59]
	v_pk_mul_f32 v[64:65], v[66:67], v[56:57]
	v_cvt_pk_bf16_f32 v54, v60, v61
	v_cvt_pk_bf16_f32 v55, v62, v63
	v_cvt_pk_bf16_f32 v56, v58, v59
	v_cvt_pk_bf16_f32 v57, v64, v65
	v_add_co_u32_e32 v62, vcc, s19, v78
	global_store_dwordx4 v[76:77], v[54:57], off
	s_nop 0
	v_addc_co_u32_e32 v63, vcc, 0, v79, vcc
	s_nop 0
	s_nop 0
	v_lshlrev_b64 v[70:71], 12, v[74:75]
	s_nop 0
	v_pk_mul_f32 v[72:73], v[16:17], v[42:43]
	v_pk_mul_f32 v[74:75], v[18:19], v[44:45]
	v_pk_mul_f32 v[76:77], v[20:21], v[46:47]
	v_pk_mul_f32 v[78:79], v[22:23], v[48:49]
	v_pk_fma_f32 v[72:73], v[12:13], v[40:41], v[72:73]
	v_pk_fma_f32 v[74:75], v[14:15], v[38:39], v[74:75]
	v_pk_fma_f32 v[76:77], v[8:9], v[36:37], v[76:77]
	v_pk_fma_f32 v[78:79], v[10:11], v[34:35], v[78:79]
	v_or_b32_e32 v66, 2, v30
	v_mad_i64_i32 v[68:69], s[16:17], v66, s20, v[32:33]
	v_lshl_add_u64 v[68:69], v[68:69], 0, v[26:27]
	v_lshl_add_u64 v[70:71], v[28:29], 0, v[70:71]
	v_ashrrev_i32_e32 v67, 31, v66
	v_lshlrev_b64 v[66:67], 12, v[66:67]
	v_lshl_add_u64 v[66:67], v[28:29], 0, v[66:67]
	s_waitcnt vmcnt(20)
; __device__ __forceinline__ u32x4 pack8(const float (&v)[8]) { u32x4 w; w.x = pk2(v[0], v[1]); w.y = pk2(v[2], v[3]); w.z = pk2(v[4], v[5]); w.w = pk2(v[6], v[7]); return w; }
; __device__ __forceinline__ void ph_conv_hglocal(const Ctx& c) {
;     ...
;             for (int tt = 0; tt < 8; ++tt) {
;                 const size_t ro = (size_t)(t0 + tt) * NIN; float ab[8], ac[8], ah[8], o[8];
;                 unpack8(*(const u32x4*)(Z + ro + ch), ab); unpack8(*(const u32x4*)(Z + ro + 1024 + ch), ac); unpack8(*(const u32x4*)(Z + ro + 2048 + ch), ah);
; #pragma unroll
;                 for (int j = 0; j < 8; ++j) { const float u0 = ac[j] * ah[j]; o[j] = ab[j] * (w0[j] * um2[j] + w1[j] * um1[j] + w2[j] * u0); um2[j] = um1[j]; um1[j] = u0; }
;                 *(u32x4*)(Y + (size_t)(t0 + tt) * D_ + ch) = pack8(o);
;             }
	v_mov_b32_e32 v54, v112
	v_mov_b32_e32 v55, v113
	v_mov_b32_e32 v56, v114
	v_mov_b32_e32 v57, v115
	v_lshlrev_b32_e32 v80, 16, v54
	s_waitcnt vmcnt(19)
	v_mov_b32_e32 v58, v116
	v_mov_b32_e32 v59, v117
	v_mov_b32_e32 v60, v118
	v_mov_b32_e32 v61, v119
	v_lshlrev_b32_e32 v34, 16, v58
	v_and_b32_e32 v35, 0xffff0000, v58
	s_waitcnt vmcnt(18)
	v_mov_b32_e32 v62, v120
	v_mov_b32_e32 v63, v121
	v_mov_b32_e32 v64, v122
	v_mov_b32_e32 v65, v123
	v_lshlrev_b32_e32 v36, 16, v62
	v_and_b32_e32 v37, 0xffff0000, v62
	v_lshlrev_b32_e32 v38, 16, v59
	v_and_b32_e32 v39, 0xffff0000, v59
	v_lshlrev_b32_e32 v40, 16, v63
	v_and_b32_e32 v41, 0xffff0000, v63
	v_lshlrev_b32_e32 v62, 16, v60
	v_and_b32_e32 v63, 0xffff0000, v60
	v_lshlrev_b32_e32 v82, 16, v64
	v_and_b32_e32 v83, 0xffff0000, v64
	v_lshlrev_b32_e32 v60, 16, v61
	v_and_b32_e32 v61, 0xffff0000, v61
	v_lshlrev_b32_e32 v64, 16, v65
	v_and_b32_e32 v65, 0xffff0000, v65
	v_pk_mul_f32 v[34:35], v[34:35], v[36:37]
	v_pk_mul_f32 v[36:37], v[38:39], v[40:41]
	v_pk_mul_f32 v[38:39], v[62:63], v[82:83]
	v_pk_mul_f32 v[40:41], v[60:61], v[64:65]
	v_and_b32_e32 v81, 0xffff0000, v54
	v_lshlrev_b32_e32 v54, 16, v55
	v_and_b32_e32 v55, 0xffff0000, v55
	v_lshlrev_b32_e32 v58, 16, v56
	v_and_b32_e32 v59, 0xffff0000, v56
	v_lshlrev_b32_e32 v56, 16, v57
	v_and_b32_e32 v57, 0xffff0000, v57
	v_pk_fma_f32 v[60:61], v[4:5], v[34:35], v[72:73]
	v_pk_fma_f32 v[62:63], v[6:7], v[36:37], v[74:75]
	v_pk_fma_f32 v[64:65], v[0:1], v[38:39], v[76:77]
	v_pk_fma_f32 v[72:73], v[2:3], v[40:41], v[78:79]
	v_pk_mul_f32 v[60:61], v[60:61], v[80:81]
	v_pk_mul_f32 v[62:63], v[62:63], v[54:55]
	v_pk_mul_f32 v[58:59], v[64:65], v[58:59]
	v_pk_mul_f32 v[64:65], v[72:73], v[56:57]
	v_cvt_pk_bf16_f32 v54, v60, v61
	v_cvt_pk_bf16_f32 v55, v62, v63
	v_cvt_pk_bf16_f32 v56, v58, v59
	v_cvt_pk_bf16_f32 v57, v64, v65
	v_add_co_u32_e32 v62, vcc, s19, v68
	global_store_dwordx4 v[70:71], v[54:57], off
	s_nop 0
	v_addc_co_u32_e32 v63, vcc, 0, v69, vcc
	s_nop 0
	s_nop 0
	v_pk_mul_f32 v[72:73], v[16:17], v[34:35]
	s_nop 0
	v_pk_mul_f32 v[74:75], v[18:19], v[36:37]
	v_pk_mul_f32 v[76:77], v[20:21], v[38:39]
	v_pk_mul_f32 v[78:79], v[22:23], v[40:41]
	v_pk_fma_f32 v[72:73], v[12:13], v[42:43], v[72:73]
	v_pk_fma_f32 v[74:75], v[14:15], v[44:45], v[74:75]
	v_pk_fma_f32 v[76:77], v[8:9], v[46:47], v[76:77]
	v_pk_fma_f32 v[78:79], v[10:11], v[48:49], v[78:79]
	v_or_b32_e32 v68, 3, v30
	v_mad_i64_i32 v[70:71], s[16:17], v68, s20, v[32:33]
	v_lshl_add_u64 v[70:71], v[70:71], 0, v[26:27]
	v_ashrrev_i32_e32 v69, 31, v68
	v_lshlrev_b64 v[68:69], 12, v[68:69]
	v_lshl_add_u64 v[68:69], v[28:29], 0, v[68:69]
	s_waitcnt vmcnt(17)
	v_mov_b32_e32 v54, v124
	v_mov_b32_e32 v55, v125
	v_mov_b32_e32 v56, v126
	v_mov_b32_e32 v57, v127
	v_lshlrev_b32_e32 v80, 16, v54
	s_waitcnt vmcnt(16)
	v_mov_b32_e32 v58, v128
	v_mov_b32_e32 v59, v129
	v_mov_b32_e32 v60, v130
	v_mov_b32_e32 v61, v131
	v_lshlrev_b32_e32 v42, 16, v58
	v_and_b32_e32 v43, 0xffff0000, v58
	s_waitcnt vmcnt(15)
	v_mov_b32_e32 v62, v132
	v_mov_b32_e32 v63, v133
	v_mov_b32_e32 v64, v134
	v_mov_b32_e32 v65, v135
	v_lshlrev_b32_e32 v44, 16, v62
	v_and_b32_e32 v45, 0xffff0000, v62
	v_lshlrev_b32_e32 v46, 16, v59
	v_and_b32_e32 v47, 0xffff0000, v59
	v_lshlrev_b32_e32 v48, 16, v63
	v_and_b32_e32 v49, 0xffff0000, v63
	v_lshlrev_b32_e32 v62, 16, v60
	v_and_b32_e32 v63, 0xffff0000, v60
	v_lshlrev_b32_e32 v82, 16, v64
	v_and_b32_e32 v83, 0xffff0000, v64
	v_lshlrev_b32_e32 v60, 16, v61
	v_and_b32_e32 v61, 0xffff0000, v61
	v_lshlrev_b32_e32 v64, 16, v65
	v_and_b32_e32 v65, 0xffff0000, v65
	v_pk_mul_f32 v[42:43], v[42:43], v[44:45]
	v_pk_mul_f32 v[44:45], v[46:47], v[48:49]
	v_pk_mul_f32 v[46:47], v[62:63], v[82:83]
	v_pk_mul_f32 v[48:49], v[60:61], v[64:65]
	v_and_b32_e32 v81, 0xffff0000, v54
	v_lshlrev_b32_e32 v54, 16, v55
	v_and_b32_e32 v55, 0xffff0000, v55
	v_lshlrev_b32_e32 v58, 16, v56
	v_and_b32_e32 v59, 0xffff0000, v56
	v_lshlrev_b32_e32 v56, 16, v57
	v_and_b32_e32 v57, 0xffff0000, v57
	v_pk_fma_f32 v[60:61], v[4:5], v[42:43], v[72:73]
	v_pk_fma_f32 v[62:63], v[6:7], v[44:45], v[74:75]
	v_pk_fma_f32 v[64:65], v[0:1], v[46:47], v[76:77]
	v_pk_fma_f32 v[72:73], v[2:3], v[48:49], v[78:79]
	v_pk_mul_f32 v[60:61], v[60:61], v[80:81]
	v_pk_mul_f32 v[62:63], v[62:63], v[54:55]
	v_pk_mul_f32 v[58:59], v[64:65], v[58:59]
	v_pk_mul_f32 v[64:65], v[72:73], v[56:57]
	v_cvt_pk_bf16_f32 v54, v60, v61
	v_cvt_pk_bf16_f32 v55, v62, v63
	v_cvt_pk_bf16_f32 v56, v58, v59
	v_cvt_pk_bf16_f32 v57, v64, v65
	v_add_co_u32_e32 v62, vcc, s19, v70
	global_store_dwordx4 v[66:67], v[54:57], off
	s_nop 0
	v_addc_co_u32_e32 v63, vcc, 0, v71, vcc
	s_nop 0
	s_nop 0
	v_pk_mul_f32 v[72:73], v[16:17], v[42:43]
	s_nop 0
	v_pk_mul_f32 v[74:75], v[18:19], v[44:45]
	v_pk_mul_f32 v[76:77], v[20:21], v[46:47]
	v_pk_mul_f32 v[78:79], v[22:23], v[48:49]
	v_pk_fma_f32 v[72:73], v[12:13], v[34:35], v[72:73]
	v_pk_fma_f32 v[74:75], v[14:15], v[36:37], v[74:75]
	v_pk_fma_f32 v[76:77], v[8:9], v[38:39], v[76:77]
	v_pk_fma_f32 v[78:79], v[10:11], v[40:41], v[78:79]
	v_or_b32_e32 v66, 4, v30
	v_mad_i64_i32 v[70:71], s[16:17], v66, s20, v[32:33]
	v_lshl_add_u64 v[70:71], v[70:71], 0, v[26:27]
	v_ashrrev_i32_e32 v67, 31, v66
	v_lshlrev_b64 v[66:67], 12, v[66:67]
	v_lshl_add_u64 v[66:67], v[28:29], 0, v[66:67]
	s_waitcnt vmcnt(14)
	v_mov_b32_e32 v54, v136
	v_mov_b32_e32 v55, v137
	v_mov_b32_e32 v56, v138
	v_mov_b32_e32 v57, v139
	v_lshlrev_b32_e32 v80, 16, v54
	s_waitcnt vmcnt(13)
	v_mov_b32_e32 v58, v140
	v_mov_b32_e32 v59, v141
	v_mov_b32_e32 v60, v142
	v_mov_b32_e32 v61, v143
	v_lshlrev_b32_e32 v34, 16, v58
	v_and_b32_e32 v35, 0xffff0000, v58
	s_waitcnt vmcnt(12)
; __device__ __forceinline__ u32x4 pack8(const float (&v)[8]) { u32x4 w; w.x = pk2(v[0], v[1]); w.y = pk2(v[2], v[3]); w.z = pk2(v[4], v[5]); w.w = pk2(v[6], v[7]); return w; }
; __device__ __forceinline__ void ph_conv_hglocal(const Ctx& c) {
;     ...
;             for (int tt = 0; tt < 8; ++tt) {
;                 const size_t ro = (size_t)(t0 + tt) * NIN; float ab[8], ac[8], ah[8], o[8];
;                 unpack8(*(const u32x4*)(Z + ro + ch), ab); unpack8(*(const u32x4*)(Z + ro + 1024 + ch), ac); unpack8(*(const u32x4*)(Z + ro + 2048 + ch), ah);
; #pragma unroll
;                 for (int j = 0; j < 8; ++j) { const float u0 = ac[j] * ah[j]; o[j] = ab[j] * (w0[j] * um2[j] + w1[j] * um1[j] + w2[j] * u0); um2[j] = um1[j]; um1[j] = u0; }
;                 *(u32x4*)(Y + (size_t)(t0 + tt) * D_ + ch) = pack8(o);
;             }
	v_mov_b32_e32 v62, v144
	v_mov_b32_e32 v63, v145
	v_mov_b32_e32 v64, v146
	v_mov_b32_e32 v65, v147
	v_lshlrev_b32_e32 v36, 16, v62
	v_and_b32_e32 v37, 0xffff0000, v62
	v_lshlrev_b32_e32 v38, 16, v59
	v_and_b32_e32 v39, 0xffff0000, v59
	v_lshlrev_b32_e32 v40, 16, v63
	v_and_b32_e32 v41, 0xffff0000, v63
	v_lshlrev_b32_e32 v62, 16, v60
	v_and_b32_e32 v63, 0xffff0000, v60
	v_lshlrev_b32_e32 v82, 16, v64
	v_and_b32_e32 v83, 0xffff0000, v64
	v_lshlrev_b32_e32 v60, 16, v61
	v_and_b32_e32 v61, 0xffff0000, v61
	v_lshlrev_b32_e32 v64, 16, v65
	v_and_b32_e32 v65, 0xffff0000, v65
	v_pk_mul_f32 v[34:35], v[34:35], v[36:37]
	v_pk_mul_f32 v[36:37], v[38:39], v[40:41]
	v_pk_mul_f32 v[38:39], v[62:63], v[82:83]
	v_pk_mul_f32 v[40:41], v[60:61], v[64:65]
	v_and_b32_e32 v81, 0xffff0000, v54
	v_lshlrev_b32_e32 v54, 16, v55
	v_and_b32_e32 v55, 0xffff0000, v55
	v_lshlrev_b32_e32 v58, 16, v56
	v_and_b32_e32 v59, 0xffff0000, v56
	v_lshlrev_b32_e32 v56, 16, v57
	v_and_b32_e32 v57, 0xffff0000, v57
	v_pk_fma_f32 v[60:61], v[4:5], v[34:35], v[72:73]
	v_pk_fma_f32 v[62:63], v[6:7], v[36:37], v[74:75]
	v_pk_fma_f32 v[64:65], v[0:1], v[38:39], v[76:77]
	v_pk_fma_f32 v[72:73], v[2:3], v[40:41], v[78:79]
	v_pk_mul_f32 v[60:61], v[60:61], v[80:81]
	v_pk_mul_f32 v[62:63], v[62:63], v[54:55]
	v_pk_mul_f32 v[58:59], v[64:65], v[58:59]
	v_pk_mul_f32 v[64:65], v[72:73], v[56:57]
	v_cvt_pk_bf16_f32 v54, v60, v61
	v_cvt_pk_bf16_f32 v55, v62, v63
	v_cvt_pk_bf16_f32 v56, v58, v59
	v_cvt_pk_bf16_f32 v57, v64, v65
	v_add_co_u32_e32 v62, vcc, s19, v70
	global_store_dwordx4 v[68:69], v[54:57], off
	s_nop 0
	v_addc_co_u32_e32 v63, vcc, 0, v71, vcc
	s_nop 0
	s_nop 0
	v_pk_mul_f32 v[72:73], v[16:17], v[34:35]
	s_nop 0
	v_pk_mul_f32 v[74:75], v[18:19], v[36:37]
	v_pk_mul_f32 v[76:77], v[20:21], v[38:39]
	v_pk_mul_f32 v[78:79], v[22:23], v[40:41]
	v_pk_fma_f32 v[72:73], v[12:13], v[42:43], v[72:73]
	v_pk_fma_f32 v[74:75], v[14:15], v[44:45], v[74:75]
	v_pk_fma_f32 v[76:77], v[8:9], v[46:47], v[76:77]
	v_pk_fma_f32 v[78:79], v[10:11], v[48:49], v[78:79]
	v_or_b32_e32 v68, 5, v30
	v_mad_i64_i32 v[70:71], s[16:17], v68, s20, v[32:33]
	v_lshl_add_u64 v[70:71], v[70:71], 0, v[26:27]
	v_ashrrev_i32_e32 v69, 31, v68
	v_lshlrev_b64 v[68:69], 12, v[68:69]
	v_lshl_add_u64 v[68:69], v[28:29], 0, v[68:69]
	s_waitcnt vmcnt(11)
	v_mov_b32_e32 v54, v148
	v_mov_b32_e32 v55, v149
	v_mov_b32_e32 v56, v150
	v_mov_b32_e32 v57, v151
	v_lshlrev_b32_e32 v80, 16, v54
	s_waitcnt vmcnt(10)
	v_mov_b32_e32 v58, v152
	v_mov_b32_e32 v59, v153
	v_mov_b32_e32 v60, v154
	v_mov_b32_e32 v61, v155
	v_lshlrev_b32_e32 v42, 16, v58
	v_and_b32_e32 v43, 0xffff0000, v58
	s_waitcnt vmcnt(9)
	v_mov_b32_e32 v62, v156
	v_mov_b32_e32 v63, v157
	v_mov_b32_e32 v64, v158
	v_mov_b32_e32 v65, v159
	v_lshlrev_b32_e32 v44, 16, v62
	v_and_b32_e32 v45, 0xffff0000, v62
	v_lshlrev_b32_e32 v46, 16, v59
	v_and_b32_e32 v47, 0xffff0000, v59
	v_lshlrev_b32_e32 v48, 16, v63
	v_and_b32_e32 v49, 0xffff0000, v63
	v_lshlrev_b32_e32 v62, 16, v60
	v_and_b32_e32 v63, 0xffff0000, v60
	v_lshlrev_b32_e32 v82, 16, v64
	v_and_b32_e32 v83, 0xffff0000, v64
	v_lshlrev_b32_e32 v60, 16, v61
	v_and_b32_e32 v61, 0xffff0000, v61
	v_lshlrev_b32_e32 v64, 16, v65
	v_and_b32_e32 v65, 0xffff0000, v65
	v_pk_mul_f32 v[42:43], v[42:43], v[44:45]
	v_pk_mul_f32 v[44:45], v[46:47], v[48:49]
	v_pk_mul_f32 v[46:47], v[62:63], v[82:83]
	v_pk_mul_f32 v[48:49], v[60:61], v[64:65]
	v_and_b32_e32 v81, 0xffff0000, v54
	v_lshlrev_b32_e32 v54, 16, v55
	v_and_b32_e32 v55, 0xffff0000, v55
	v_lshlrev_b32_e32 v58, 16, v56
	v_and_b32_e32 v59, 0xffff0000, v56
	v_lshlrev_b32_e32 v56, 16, v57
	v_and_b32_e32 v57, 0xffff0000, v57
	v_pk_fma_f32 v[60:61], v[4:5], v[42:43], v[72:73]
	v_pk_fma_f32 v[62:63], v[6:7], v[44:45], v[74:75]
	v_pk_fma_f32 v[64:65], v[0:1], v[46:47], v[76:77]
	v_pk_fma_f32 v[72:73], v[2:3], v[48:49], v[78:79]
	v_pk_mul_f32 v[60:61], v[60:61], v[80:81]
	v_pk_mul_f32 v[62:63], v[62:63], v[54:55]
	v_pk_mul_f32 v[58:59], v[64:65], v[58:59]
	v_pk_mul_f32 v[64:65], v[72:73], v[56:57]
	v_cvt_pk_bf16_f32 v54, v60, v61
	v_cvt_pk_bf16_f32 v55, v62, v63
	v_cvt_pk_bf16_f32 v56, v58, v59
	v_cvt_pk_bf16_f32 v57, v64, v65
	v_add_co_u32_e32 v62, vcc, s19, v70
	global_store_dwordx4 v[66:67], v[54:57], off
	s_nop 0
	v_addc_co_u32_e32 v63, vcc, 0, v71, vcc
	s_nop 0
	s_nop 0
	v_or_b32_e32 v66, 6, v30
	s_nop 0
	v_mad_i64_i32 v[30:31], s[16:17], v66, s20, v[32:33]
	v_lshl_add_u64 v[70:71], v[30:31], 0, v[26:27]
	v_pk_mul_f32 v[30:31], v[16:17], v[42:43]
	v_pk_mul_f32 v[72:73], v[18:19], v[44:45]
	v_pk_mul_f32 v[74:75], v[20:21], v[46:47]
	v_pk_mul_f32 v[76:77], v[22:23], v[48:49]
	v_pk_fma_f32 v[78:79], v[12:13], v[34:35], v[30:31]
	v_pk_fma_f32 v[72:73], v[14:15], v[36:37], v[72:73]
	v_pk_fma_f32 v[74:75], v[8:9], v[38:39], v[74:75]
	v_pk_fma_f32 v[40:41], v[10:11], v[40:41], v[76:77]
	v_ashrrev_i32_e32 v67, 31, v66
	s_waitcnt vmcnt(8)
	v_mov_b32_e32 v54, v160
	v_mov_b32_e32 v55, v161
	v_mov_b32_e32 v56, v162
	v_mov_b32_e32 v57, v163
	v_lshlrev_b32_e32 v76, 16, v54
	s_waitcnt vmcnt(7)
	v_mov_b32_e32 v58, v164
	v_mov_b32_e32 v59, v165
	v_mov_b32_e32 v60, v166
	v_mov_b32_e32 v61, v167
	v_lshlrev_b32_e32 v30, 16, v58
	v_and_b32_e32 v31, 0xffff0000, v58
	s_waitcnt vmcnt(6)
; __device__ __forceinline__ u32x4 pack8(const float (&v)[8]) { u32x4 w; w.x = pk2(v[0], v[1]); w.y = pk2(v[2], v[3]); w.z = pk2(v[4], v[5]); w.w = pk2(v[6], v[7]); return w; }
; __device__ __forceinline__ void ph_conv_hglocal(const Ctx& c) {
;     ...
;             for (int tt = 0; tt < 8; ++tt) {
;                 const size_t ro = (size_t)(t0 + tt) * NIN; float ab[8], ac[8], ah[8], o[8];
;                 unpack8(*(const u32x4*)(Z + ro + ch), ab); unpack8(*(const u32x4*)(Z + ro + 1024 + ch), ac); unpack8(*(const u32x4*)(Z + ro + 2048 + ch), ah);
; #pragma unroll
;                 for (int j = 0; j < 8; ++j) { const float u0 = ac[j] * ah[j]; o[j] = ab[j] * (w0[j] * um2[j] + w1[j] * um1[j] + w2[j] * u0); um2[j] = um1[j]; um1[j] = u0; }
;                 *(u32x4*)(Y + (size_t)(t0 + tt) * D_ + ch) = pack8(o);
;             }
	v_mov_b32_e32 v62, v168
	v_mov_b32_e32 v63, v169
	v_mov_b32_e32 v64, v170
	v_mov_b32_e32 v65, v171
	v_lshlrev_b32_e32 v34, 16, v62
	v_and_b32_e32 v35, 0xffff0000, v62
	v_lshlrev_b32_e32 v36, 16, v59
	v_and_b32_e32 v37, 0xffff0000, v59
	v_lshlrev_b32_e32 v38, 16, v63
	v_and_b32_e32 v39, 0xffff0000, v63
	v_lshlrev_b32_e32 v62, 16, v60
	v_and_b32_e32 v63, 0xffff0000, v60
	v_lshlrev_b32_e32 v80, 16, v64
	v_and_b32_e32 v81, 0xffff0000, v64
	v_lshlrev_b32_e32 v60, 16, v61
	v_and_b32_e32 v61, 0xffff0000, v61
	v_lshlrev_b32_e32 v64, 16, v65
	v_and_b32_e32 v65, 0xffff0000, v65
	v_pk_mul_f32 v[30:31], v[30:31], v[34:35]
	v_pk_mul_f32 v[34:35], v[36:37], v[38:39]
	v_pk_mul_f32 v[36:37], v[62:63], v[80:81]
	v_pk_mul_f32 v[38:39], v[60:61], v[64:65]
	v_and_b32_e32 v77, 0xffff0000, v54
	v_lshlrev_b32_e32 v54, 16, v55
	v_and_b32_e32 v55, 0xffff0000, v55
	v_lshlrev_b32_e32 v58, 16, v56
	v_and_b32_e32 v59, 0xffff0000, v56
	v_lshlrev_b32_e32 v56, 16, v57
	v_and_b32_e32 v57, 0xffff0000, v57
	v_pk_fma_f32 v[60:61], v[4:5], v[30:31], v[78:79]
	v_pk_fma_f32 v[62:63], v[6:7], v[34:35], v[72:73]
	v_pk_fma_f32 v[64:65], v[0:1], v[36:37], v[74:75]
	v_pk_fma_f32 v[40:41], v[2:3], v[38:39], v[40:41]
	v_pk_mul_f32 v[60:61], v[60:61], v[76:77]
	v_pk_mul_f32 v[62:63], v[62:63], v[54:55]
	v_pk_mul_f32 v[58:59], v[64:65], v[58:59]
	v_pk_mul_f32 v[40:41], v[40:41], v[56:57]
	v_cvt_pk_bf16_f32 v54, v60, v61
	v_cvt_pk_bf16_f32 v55, v62, v63
	v_cvt_pk_bf16_f32 v56, v58, v59
	v_cvt_pk_bf16_f32 v57, v40, v41
	v_add_co_u32_e32 v40, vcc, s19, v70
	global_store_dwordx4 v[68:69], v[54:57], off
	s_nop 0
	v_addc_co_u32_e32 v41, vcc, 0, v71, vcc
	s_nop 0
	s_nop 0
	s_nop 0
	v_lshlrev_b64 v[40:41], 12, v[66:67]
	v_or_b32_e32 v68, 7, v52
	v_lshl_add_u64 v[52:53], v[28:29], 0, v[40:41]
	v_pk_mul_f32 v[40:41], v[16:17], v[30:31]
	v_pk_mul_f32 v[66:67], v[18:19], v[34:35]
	v_pk_mul_f32 v[70:71], v[20:21], v[36:37]
	v_pk_mul_f32 v[72:73], v[22:23], v[38:39]
	v_pk_fma_f32 v[40:41], v[12:13], v[42:43], v[40:41]
	v_pk_fma_f32 v[42:43], v[14:15], v[44:45], v[66:67]
	v_pk_fma_f32 v[44:45], v[8:9], v[46:47], v[70:71]
	v_pk_fma_f32 v[46:47], v[10:11], v[48:49], v[72:73]
	v_mad_i64_i32 v[32:33], s[16:17], v68, s20, v[32:33]
	v_lshl_add_u64 v[32:33], v[32:33], 0, v[26:27]
	v_ashrrev_i32_e32 v69, 31, v68
	s_waitcnt vmcnt(5)
	v_mov_b32_e32 v54, v172
	v_mov_b32_e32 v55, v173
	v_mov_b32_e32 v56, v174
	v_mov_b32_e32 v57, v175
	v_lshlrev_b32_e32 v48, 16, v54
	s_waitcnt vmcnt(4)
	v_mov_b32_e32 v58, v176
	v_mov_b32_e32 v59, v177
	v_mov_b32_e32 v60, v178
	v_mov_b32_e32 v61, v179
	v_lshlrev_b32_e32 v66, 16, v58
	v_and_b32_e32 v67, 0xffff0000, v58
	s_waitcnt vmcnt(3)
	v_mov_b32_e32 v62, v180
	v_mov_b32_e32 v63, v181
	v_mov_b32_e32 v64, v182
	v_mov_b32_e32 v65, v183
	v_lshlrev_b32_e32 v70, 16, v62
	v_and_b32_e32 v71, 0xffff0000, v62
	v_lshlrev_b32_e32 v58, 16, v59
	v_and_b32_e32 v59, 0xffff0000, v59
	v_lshlrev_b32_e32 v62, 16, v63
	v_and_b32_e32 v63, 0xffff0000, v63
	v_lshlrev_b32_e32 v74, 16, v60
	v_and_b32_e32 v75, 0xffff0000, v60
	v_lshlrev_b32_e32 v76, 16, v64
	v_and_b32_e32 v77, 0xffff0000, v64
	v_lshlrev_b32_e32 v60, 16, v61
	v_and_b32_e32 v61, 0xffff0000, v61
	v_lshlrev_b32_e32 v64, 16, v65
	v_and_b32_e32 v65, 0xffff0000, v65
	v_pk_mul_f32 v[66:67], v[66:67], v[70:71]
	v_pk_mul_f32 v[58:59], v[58:59], v[62:63]
	v_pk_mul_f32 v[62:63], v[74:75], v[76:77]
	v_pk_mul_f32 v[60:61], v[60:61], v[64:65]
	v_and_b32_e32 v49, 0xffff0000, v54
	v_lshlrev_b32_e32 v54, 16, v55
	v_and_b32_e32 v55, 0xffff0000, v55
	v_lshlrev_b32_e32 v72, 16, v56
	v_and_b32_e32 v73, 0xffff0000, v56
	v_lshlrev_b32_e32 v56, 16, v57
	v_and_b32_e32 v57, 0xffff0000, v57
	v_pk_fma_f32 v[40:41], v[4:5], v[66:67], v[40:41]
	v_pk_fma_f32 v[42:43], v[6:7], v[58:59], v[42:43]
	v_pk_fma_f32 v[44:45], v[0:1], v[62:63], v[44:45]
	v_pk_fma_f32 v[46:47], v[2:3], v[60:61], v[46:47]
	v_pk_mul_f32 v[40:41], v[40:41], v[48:49]
	v_pk_mul_f32 v[42:43], v[42:43], v[54:55]
	v_pk_mul_f32 v[44:45], v[44:45], v[72:73]
	v_pk_mul_f32 v[46:47], v[46:47], v[56:57]
	v_cvt_pk_bf16_f32 v40, v40, v41
	v_cvt_pk_bf16_f32 v41, v42, v43
	v_cvt_pk_bf16_f32 v42, v44, v45
	v_cvt_pk_bf16_f32 v43, v46, v47
	global_store_dwordx4 v[52:53], v[40:43], off
	s_nop 0
	s_nop 0
	s_nop 0
	v_add_co_u32_e32 v32, vcc, s19, v32
	v_pk_mul_f32 v[16:17], v[16:17], v[66:67]
	s_nop 0
	v_addc_co_u32_e32 v33, vcc, 0, v33, vcc
	s_nop 0
	v_lshlrev_b64 v[32:33], 12, v[68:69]
	v_pk_mul_f32 v[18:19], v[18:19], v[58:59]
	v_pk_mul_f32 v[20:21], v[20:21], v[62:63]
	v_pk_mul_f32 v[22:23], v[22:23], v[60:61]
	v_lshl_add_u64 v[28:29], v[28:29], 0, v[32:33]
	v_pk_fma_f32 v[12:13], v[12:13], v[30:31], v[16:17]
	v_pk_fma_f32 v[14:15], v[14:15], v[34:35], v[18:19]
	v_pk_fma_f32 v[8:9], v[8:9], v[36:37], v[20:21]
	v_pk_fma_f32 v[10:11], v[10:11], v[38:39], v[22:23]
	v_cmp_lt_i32_e32 vcc, s21, v25
	s_or_b64 s[8:9], vcc, s[8:9]
	s_waitcnt vmcnt(2)
	v_mov_b32_e32 v40, v184
	v_mov_b32_e32 v41, v185
	v_mov_b32_e32 v42, v186
	v_mov_b32_e32 v43, v187
	v_lshlrev_b32_e32 v16, 16, v40
	v_and_b32_e32 v17, 0xffff0000, v40
	s_waitcnt vmcnt(1)
	v_mov_b32_e32 v44, v188
	v_mov_b32_e32 v45, v189
	v_mov_b32_e32 v46, v190
	v_mov_b32_e32 v47, v191
	v_lshlrev_b32_e32 v18, 16, v44
	v_and_b32_e32 v19, 0xffff0000, v44
	v_lshlrev_b32_e32 v22, 16, v41
	v_and_b32_e32 v23, 0xffff0000, v41
	v_lshlrev_b32_e32 v30, 16, v45
	s_waitcnt vmcnt(0)
	v_mov_b32_e32 v52, v192
	v_mov_b32_e32 v53, v193
	v_mov_b32_e32 v54, v194
	v_mov_b32_e32 v55, v195
	v_lshlrev_b32_e32 v20, 16, v52
	v_and_b32_e32 v21, 0xffff0000, v52
	v_and_b32_e32 v31, 0xffff0000, v45
	v_lshlrev_b32_e32 v32, 16, v53
	v_and_b32_e32 v33, 0xffff0000, v53
	v_lshlrev_b32_e32 v34, 16, v42
	v_and_b32_e32 v35, 0xffff0000, v42
	v_lshlrev_b32_e32 v36, 16, v46
	v_and_b32_e32 v37, 0xffff0000, v46
	v_lshlrev_b32_e32 v38, 16, v54
	v_and_b32_e32 v39, 0xffff0000, v54
	v_lshlrev_b32_e32 v40, 16, v43
	v_and_b32_e32 v41, 0xffff0000, v43
	v_lshlrev_b32_e32 v42, 16, v47
	v_and_b32_e32 v43, 0xffff0000, v47
	v_lshlrev_b32_e32 v44, 16, v55
	v_and_b32_e32 v45, 0xffff0000, v55
	v_pk_mul_f32 v[18:19], v[18:19], v[20:21]
	v_pk_mul_f32 v[20:21], v[30:31], v[32:33]
	v_pk_mul_f32 v[30:31], v[36:37], v[38:39]
	v_pk_mul_f32 v[32:33], v[42:43], v[44:45]
	v_pk_fma_f32 v[4:5], v[4:5], v[18:19], v[12:13]
	v_pk_fma_f32 v[6:7], v[6:7], v[20:21], v[14:15]
	v_pk_fma_f32 v[0:1], v[0:1], v[30:31], v[8:9]
	v_pk_fma_f32 v[2:3], v[2:3], v[32:33], v[10:11]
	v_pk_mul_f32 v[4:5], v[4:5], v[16:17]
	v_pk_mul_f32 v[6:7], v[6:7], v[22:23]
	v_pk_mul_f32 v[8:9], v[0:1], v[34:35]
	v_pk_mul_f32 v[10:11], v[2:3], v[40:41]
	v_cvt_pk_bf16_f32 v0, v4, v5
	v_cvt_pk_bf16_f32 v1, v6, v7
	v_cvt_pk_bf16_f32 v2, v8, v9
	v_cvt_pk_bf16_f32 v3, v10, v11
	global_store_dwordx4 v[28:29], v[0:3], off
	s_andn2_b64 exec, exec, s[8:9]
	s_cbranch_execz .LBB0_453
